# speedup vs baseline: 1.0086x; 1.0009x over previous
_Z11proj_kernelPKfS0_PKDF16_S0_S0_PDF16_S3_:
	s_load_dwordx8 s[4:11], s[0:1], 0x0
	s_lshl_b32 s3, s2, 6
	s_add_i32 s12, s3, 0xffffe000
	s_ashr_i32 s13, s3, 31
	s_cmpk_lt_i32 s3, 0x2000
	s_cselect_b32 s13, s13, 0
	s_cselect_b32 s12, s3, s12
	s_waitcnt lgkmcnt(0)
	s_cselect_b32 s3, s5, s7
	s_cselect_b32 s6, s4, s6
	s_lshl_b64 s[4:5], s[12:13], 10
	s_add_u32 s4, s6, s4
	s_addc_u32 s5, s3, s5
	v_readfirstlane_b32 s15, v0
	v_lshlrev_b32_e32 v70, 4, v0
	v_mov_b32_e32 v71, 0
	s_movk_i32 s14, 0x2000
	v_lshl_add_u64 v[26:27], s[4:5], 0, v[70:71]
	v_add_co_u32_e32 v10, vcc, s14, v26
	s_movk_i32 s3, 0x6000
	s_nop 0
	v_addc_co_u32_e32 v11, vcc, 0, v27, vcc
	v_add_co_u32_e32 v18, vcc, s3, v26
	s_mov_b32 s6, 0xa000
	s_nop 0
	v_addc_co_u32_e32 v19, vcc, 0, v27, vcc
	v_or_b32_e32 v42, 0x400, v0
	v_add_co_u32_e32 v28, vcc, s6, v26
	v_lshlrev_b32_e32 v1, 4, v42
	v_or_b32_e32 v43, 0x800, v0
	v_addc_co_u32_e32 v29, vcc, 0, v27, vcc
	s_mov_b32 s6, 0xe000
	global_load_dwordx4 v[2:5], v[10:11], off
	global_load_dwordx4 v[6:9], v1, s[4:5]
	v_lshlrev_b32_e32 v1, 4, v43
	v_or_b32_e32 v44, 0xc00, v0
	v_add_co_u32_e32 v34, vcc, s6, v26
	global_load_dwordx4 v[10:13], v[18:19], off
	global_load_dwordx4 v[14:17], v1, s[4:5]
	v_lshlrev_b32_e32 v1, 4, v44
	global_load_dwordx4 v[18:21], v[28:29], off
	global_load_dwordx4 v[22:25], v1, s[4:5]
	v_addc_co_u32_e32 v35, vcc, 0, v27, vcc
	global_load_dwordx4 v[26:29], v70, s[4:5]
	global_load_dwordx4 v[30:33], v[34:35], off
	s_lshr_b32 s15, s15, 6
	s_cmp_lt_u32 s15, 4
	s_cbranch_scc1 .Lmy_proj_noprio
	s_setprio 1
.Lmy_proj_noprio:
	s_load_dwordx4 s[4:7], s[0:1], 0x20
	s_load_dwordx2 s[12:13], s[0:1], 0x30
	v_and_b32_e32 v73, 63, v0
	v_and_b32_e32 v1, 31, v0
	v_lshrrev_b32_e32 v76, 6, v0
	v_bfe_u32 v77, v0, 5, 1
	v_or_b32_e32 v45, 0x200, v0
	v_or_b32_e32 v46, 0x600, v0
	v_or_b32_e32 v47, 0xa00, v0
	v_or_b32_e32 v48, 0xe00, v0
	v_lshlrev_b32_e32 v34, 15, v76
	v_mov_b32_e32 v35, v71
	v_lshl_add_u64 v[34:35], s[8:9], 0, v[34:35]
	v_lshlrev_b32_e32 v36, 4, v73
	v_mov_b32_e32 v37, v71
	v_lshl_add_u64 v[68:69], v[34:35], 0, v[36:37]
	s_movk_i32 s0, 0x5000
	v_add_co_u32_e32 v38, vcc, s0, v68
	s_movk_i32 s0, 0x4000
	s_nop 0
	v_addc_co_u32_e32 v39, vcc, 0, v69, vcc
	global_load_dwordx4 v[34:37], v[68:69], off
	global_load_dwordx4 v[78:81], v[38:39], off offset:-4096
	v_add_co_u32_e32 v40, vcc, s0, v68
	s_nop 1
	v_addc_co_u32_e32 v41, vcc, 0, v69, vcc
	global_load_dwordx4 v[82:85], v[68:69], off offset:1024
	global_load_dwordx4 v[86:89], v[40:41], off offset:1024
	global_load_dwordx4 v[90:93], v[68:69], off offset:2048
	global_load_dwordx4 v[94:97], v[40:41], off offset:2048
	global_load_dwordx4 v[98:101], v[68:69], off offset:3072
	global_load_dwordx4 v[102:105], v[40:41], off offset:3072
	v_add_co_u32_e32 v74, vcc, s14, v68
	s_movk_i32 s0, 0x1000
	s_nop 0
	v_addc_co_u32_e32 v75, vcc, 0, v69, vcc
	global_load_dwordx4 v[106:109], v[74:75], off offset:-4096
	global_load_dwordx4 v[110:113], v[38:39], off
	v_add_co_u32_e32 v40, vcc, s0, v68
	s_nop 1
	v_addc_co_u32_e32 v41, vcc, 0, v69, vcc
	global_load_dwordx4 v[114:117], v[40:41], off offset:1024
	global_load_dwordx4 v[118:121], v[38:39], off offset:1024
	global_load_dwordx4 v[122:125], v[40:41], off offset:2048
	global_load_dwordx4 v[126:129], v[38:39], off offset:2048
	global_load_dwordx4 v[130:133], v[40:41], off offset:3072
	global_load_dwordx4 v[134:137], v[38:39], off offset:3072
	v_lshlrev_b32_e32 v38, 3, v0
	v_and_b32_e32 v38, 0x1f8, v38
	v_add_u32_e32 v38, 0, v38
	s_movk_i32 s0, 0x210
	s_waitcnt vmcnt(17)
	v_cvt_pk_f16_f32 v29, v28, v29
	v_cvt_pk_f16_f32 v28, v26, v27
	v_mad_u32_u24 v26, v76, s0, v38
	ds_write_b64 v26, v[28:29]
	v_lshrrev_b32_e32 v26, 6, v45
	v_cvt_pk_f16_f32 v5, v4, v5
	v_cvt_pk_f16_f32 v4, v2, v3
	v_mad_u32_u24 v2, v26, s0, v38
	ds_write_b64 v2, v[4:5]
	v_lshrrev_b32_e32 v4, 6, v42
	v_cvt_pk_f16_f32 v3, v8, v9
	v_cvt_pk_f16_f32 v2, v6, v7
	v_mad_u32_u24 v4, v4, s0, v38
	ds_write_b64 v4, v[2:3]
	v_lshrrev_b32_e32 v4, 6, v46
	v_cvt_pk_f16_f32 v3, v12, v13
	v_cvt_pk_f16_f32 v2, v10, v11
	v_mad_u32_u24 v4, v4, s0, v38
	ds_write_b64 v4, v[2:3]
	v_lshrrev_b32_e32 v4, 6, v43
	v_cvt_pk_f16_f32 v3, v16, v17
	v_cvt_pk_f16_f32 v2, v14, v15
	v_mad_u32_u24 v4, v4, s0, v38
	ds_write_b64 v4, v[2:3]
	v_lshrrev_b32_e32 v4, 6, v47
	v_cvt_pk_f16_f32 v3, v20, v21
	v_cvt_pk_f16_f32 v2, v18, v19
	v_mad_u32_u24 v4, v4, s0, v38
	ds_write_b64 v4, v[2:3]
	v_lshrrev_b32_e32 v4, 6, v44
	v_cvt_pk_f16_f32 v3, v24, v25
	v_cvt_pk_f16_f32 v2, v22, v23
	v_mad_u32_u24 v4, v4, s0, v38
	ds_write_b64 v4, v[2:3]
	v_lshrrev_b32_e32 v4, 6, v48
	s_waitcnt vmcnt(16)
	v_cvt_pk_f16_f32 v3, v32, v33
	v_cvt_pk_f16_f32 v2, v30, v31
	v_mad_u32_u24 v4, v4, s0, v38
	ds_write_b64 v4, v[2:3]
	v_mul_u32_u24_e32 v2, 0x210, v1
	v_lshlrev_b32_e32 v66, 4, v77
	v_add3_u32 v67, 0, v2, v66
	s_waitcnt lgkmcnt(0)
	s_barrier
	ds_read_b128 v[2:5], v67
	ds_read_b128 v[138:141], v67 offset:32
	ds_read_b128 v[6:9], v67 offset:16896
	ds_read_b128 v[142:145], v67 offset:16928
	s_movk_i32 s0, 0x7000
	v_add_co_u32_e32 v166, vcc, s0, v68
	s_waitcnt vmcnt(15) lgkmcnt(3)
	v_mfma_f32_32x32x16_f16 v[50:65], v[34:37], v[2:5], 0
	v_addc_co_u32_e32 v167, vcc, 0, v69, vcc
	global_load_dwordx4 v[146:149], v[74:75], off
	global_load_dwordx4 v[150:153], v[166:167], off offset:-4096
	ds_read_b128 v[154:157], v67 offset:64
	ds_read_b128 v[158:161], v67 offset:16960
	v_add_co_u32_e32 v168, vcc, s3, v68
	s_waitcnt lgkmcnt(3)
	v_mfma_f32_32x32x16_f16 v[34:49], v[34:37], v[6:9], 0
	v_addc_co_u32_e32 v169, vcc, 0, v69, vcc
	s_waitcnt vmcnt(16)
	v_mfma_f32_32x32x16_f16 v[18:33], v[78:81], v[2:5], 0
	v_mfma_f32_32x32x16_f16 v[2:17], v[78:81], v[6:9], 0
	s_waitcnt vmcnt(15)
	v_mfma_f32_32x32x16_f16 v[50:65], v[82:85], v[138:141], v[50:65]
	s_waitcnt lgkmcnt(2)
	v_mfma_f32_32x32x16_f16 v[34:49], v[82:85], v[142:145], v[34:49]
	global_load_dwordx4 v[78:81], v[74:75], off offset:1024
	global_load_dwordx4 v[82:85], v[168:169], off offset:1024
	s_waitcnt vmcnt(16)
	v_mfma_f32_32x32x16_f16 v[2:17], v[86:89], v[142:145], v[2:17]
	v_mfma_f32_32x32x16_f16 v[18:33], v[86:89], v[138:141], v[18:33]
	ds_read_b128 v[138:141], v67 offset:96
	ds_read_b128 v[162:165], v67 offset:16992
	s_waitcnt vmcnt(15) lgkmcnt(3)
	v_mfma_f32_32x32x16_f16 v[50:65], v[90:93], v[154:157], v[50:65]
	s_waitcnt lgkmcnt(2)
	v_mfma_f32_32x32x16_f16 v[34:49], v[90:93], v[158:161], v[34:49]
	global_load_dwordx4 v[86:89], v[74:75], off offset:2048
	global_load_dwordx4 v[90:93], v[168:169], off offset:2048
	s_waitcnt vmcnt(16)
	v_mfma_f32_32x32x16_f16 v[2:17], v[94:97], v[158:161], v[2:17]
	v_mfma_f32_32x32x16_f16 v[18:33], v[94:97], v[154:157], v[18:33]
	ds_read_b128 v[142:145], v67 offset:128
	ds_read_b128 v[154:157], v67 offset:17024
	s_waitcnt vmcnt(15) lgkmcnt(3)
	v_mfma_f32_32x32x16_f16 v[50:65], v[98:101], v[138:141], v[50:65]
	s_waitcnt lgkmcnt(2)
	v_mfma_f32_32x32x16_f16 v[34:49], v[98:101], v[162:165], v[34:49]
	global_load_dwordx4 v[94:97], v[74:75], off offset:3072
	global_load_dwordx4 v[98:101], v[168:169], off offset:3072
	s_waitcnt vmcnt(16)
	v_mfma_f32_32x32x16_f16 v[2:17], v[102:105], v[162:165], v[2:17]
	v_mfma_f32_32x32x16_f16 v[18:33], v[102:105], v[138:141], v[18:33]
	ds_read_b128 v[138:141], v67 offset:160
	ds_read_b128 v[158:161], v67 offset:17056
	s_movk_i32 s0, 0x3000
	v_add_co_u32_e32 v68, vcc, s0, v68
	s_waitcnt vmcnt(15) lgkmcnt(3)
	v_mfma_f32_32x32x16_f16 v[50:65], v[106:109], v[142:145], v[50:65]
	v_addc_co_u32_e32 v69, vcc, 0, v69, vcc
	s_waitcnt lgkmcnt(2)
	v_mfma_f32_32x32x16_f16 v[34:49], v[106:109], v[154:157], v[34:49]
	global_load_dwordx4 v[102:105], v[68:69], off
	global_load_dwordx4 v[106:109], v[166:167], off
	s_waitcnt vmcnt(16)
	v_mfma_f32_32x32x16_f16 v[2:17], v[110:113], v[154:157], v[2:17]
	v_mfma_f32_32x32x16_f16 v[18:33], v[110:113], v[142:145], v[18:33]
	ds_read_b128 v[142:145], v67 offset:192
	ds_read_b128 v[162:165], v67 offset:17088
	s_waitcnt vmcnt(15) lgkmcnt(3)
	v_mfma_f32_32x32x16_f16 v[50:65], v[114:117], v[138:141], v[50:65]
	s_waitcnt lgkmcnt(2)
	v_mfma_f32_32x32x16_f16 v[34:49], v[114:117], v[158:161], v[34:49]
	global_load_dwordx4 v[110:113], v[68:69], off offset:1024
	global_load_dwordx4 v[114:117], v[166:167], off offset:1024
	s_waitcnt vmcnt(16)
	v_mfma_f32_32x32x16_f16 v[2:17], v[118:121], v[158:161], v[2:17]
	v_mfma_f32_32x32x16_f16 v[18:33], v[118:121], v[138:141], v[18:33]
	ds_read_b128 v[138:141], v67 offset:224
	ds_read_b128 v[154:157], v67 offset:17120
	s_waitcnt vmcnt(15) lgkmcnt(3)
	v_mfma_f32_32x32x16_f16 v[50:65], v[122:125], v[142:145], v[50:65]
	s_waitcnt lgkmcnt(2)
	v_mfma_f32_32x32x16_f16 v[34:49], v[122:125], v[162:165], v[34:49]
	global_load_dwordx4 v[118:121], v[68:69], off offset:2048
	global_load_dwordx4 v[122:125], v[166:167], off offset:2048
	s_waitcnt vmcnt(16)
	v_mfma_f32_32x32x16_f16 v[2:17], v[126:129], v[162:165], v[2:17]
	v_mfma_f32_32x32x16_f16 v[18:33], v[126:129], v[142:145], v[18:33]
	ds_read_b128 v[142:145], v67 offset:256
	ds_read_b128 v[158:161], v67 offset:17152
	s_waitcnt vmcnt(15) lgkmcnt(3)
	v_mfma_f32_32x32x16_f16 v[50:65], v[130:133], v[138:141], v[50:65]
	s_waitcnt lgkmcnt(2)
	v_mfma_f32_32x32x16_f16 v[34:49], v[130:133], v[154:157], v[34:49]
	global_load_dwordx4 v[126:129], v[68:69], off offset:3072
	global_load_dwordx4 v[130:133], v[166:167], off offset:3072
	s_waitcnt vmcnt(16)
	v_mfma_f32_32x32x16_f16 v[2:17], v[134:137], v[154:157], v[2:17]
	v_mfma_f32_32x32x16_f16 v[18:33], v[134:137], v[138:141], v[18:33]
	ds_read_b128 v[138:141], v67 offset:288
	ds_read_b128 v[162:165], v67 offset:17184
	s_waitcnt vmcnt(14) lgkmcnt(2)
	v_mfma_f32_32x32x16_f16 v[2:17], v[150:153], v[158:161], v[2:17]
	v_mfma_f32_32x32x16_f16 v[50:65], v[146:149], v[142:145], v[50:65]
	v_mfma_f32_32x32x16_f16 v[18:33], v[150:153], v[142:145], v[18:33]
	ds_read_b128 v[134:137], v67 offset:320
	ds_read_b128 v[142:145], v67 offset:17216
	v_mfma_f32_32x32x16_f16 v[34:49], v[146:149], v[158:161], v[34:49]
	s_waitcnt vmcnt(12) lgkmcnt(2)
	v_mfma_f32_32x32x16_f16 v[2:17], v[82:85], v[162:165], v[2:17]
	v_mfma_f32_32x32x16_f16 v[50:65], v[78:81], v[138:141], v[50:65]
	v_mfma_f32_32x32x16_f16 v[34:49], v[78:81], v[162:165], v[34:49]
	v_mfma_f32_32x32x16_f16 v[18:33], v[82:85], v[138:141], v[18:33]
	ds_read_b128 v[78:81], v67 offset:352
	ds_read_b128 v[138:141], v67 offset:17248
	s_waitcnt vmcnt(10) lgkmcnt(2)
	v_mfma_f32_32x32x16_f16 v[2:17], v[90:93], v[142:145], v[2:17]
	v_mfma_f32_32x32x16_f16 v[50:65], v[86:89], v[134:137], v[50:65]
	v_mfma_f32_32x32x16_f16 v[34:49], v[86:89], v[142:145], v[34:49]
	ds_read_b128 v[82:85], v67 offset:384
	ds_read_b128 v[86:89], v67 offset:17280
	v_mfma_f32_32x32x16_f16 v[18:33], v[90:93], v[134:137], v[18:33]
	s_waitcnt vmcnt(8) lgkmcnt(2)
	v_mfma_f32_32x32x16_f16 v[2:17], v[98:101], v[138:141], v[2:17]
	v_mfma_f32_32x32x16_f16 v[50:65], v[94:97], v[78:81], v[50:65]
	v_mfma_f32_32x32x16_f16 v[18:33], v[98:101], v[78:81], v[18:33]
	ds_read_b128 v[78:81], v67 offset:416
	ds_read_b128 v[90:93], v67 offset:17312
	v_mfma_f32_32x32x16_f16 v[34:49], v[94:97], v[138:141], v[34:49]
	s_waitcnt vmcnt(6) lgkmcnt(2)
	v_mfma_f32_32x32x16_f16 v[2:17], v[106:109], v[86:89], v[2:17]
	v_mfma_f32_32x32x16_f16 v[50:65], v[102:105], v[82:85], v[50:65]
	v_mfma_f32_32x32x16_f16 v[18:33], v[106:109], v[82:85], v[18:33]
	ds_read_b128 v[82:85], v67 offset:448
	ds_read_b128 v[94:97], v67 offset:17344
	v_mfma_f32_32x32x16_f16 v[34:49], v[102:105], v[86:89], v[34:49]
	s_waitcnt vmcnt(4) lgkmcnt(2)
	v_mfma_f32_32x32x16_f16 v[2:17], v[114:117], v[90:93], v[2:17]
	v_mfma_f32_32x32x16_f16 v[50:65], v[110:113], v[78:81], v[50:65]
	v_mfma_f32_32x32x16_f16 v[18:33], v[114:117], v[78:81], v[18:33]
	ds_read_b128 v[78:81], v67 offset:480
	ds_read_b128 v[86:89], v67 offset:17376
	v_mfma_f32_32x32x16_f16 v[34:49], v[110:113], v[90:93], v[34:49]
	s_waitcnt vmcnt(2) lgkmcnt(2)
	v_mfma_f32_32x32x16_f16 v[2:17], v[122:125], v[94:97], v[2:17]
	v_mfma_f32_32x32x16_f16 v[50:65], v[118:121], v[82:85], v[50:65]
	v_mfma_f32_32x32x16_f16 v[34:49], v[118:121], v[94:97], v[34:49]
	v_mfma_f32_32x32x16_f16 v[18:33], v[122:125], v[82:85], v[18:33]
	s_waitcnt vmcnt(0) lgkmcnt(0)
	v_mfma_f32_32x32x16_f16 v[2:17], v[130:133], v[86:89], v[2:17]
	v_mfma_f32_32x32x16_f16 v[50:65], v[126:129], v[78:81], v[50:65]
	v_mfma_f32_32x32x16_f16 v[34:49], v[126:129], v[86:89], v[34:49]
	v_mfma_f32_32x32x16_f16 v[18:33], v[130:133], v[78:81], v[18:33]
	v_and_b32_e32 v98, 0x1c0, v0
	v_and_b32_e32 v67, 0xc0, v0
	v_lshlrev_b32_e32 v74, 2, v98
	v_mov_b32_e32 v75, v71
	s_movk_i32 s0, 0xfc00
	s_movk_i32 s3, 0x100
	v_lshlrev_b32_e32 v68, 2, v67
	v_mov_b32_e32 v69, v71
	v_lshl_add_u64 v[74:75], s[4:5], 0, v[74:75]
	s_mov_b32 s1, -1
	v_lshl_add_u64 v[68:69], s[10:11], 0, v[68:69]
	v_lshl_add_u64 v[74:75], v[74:75], 0, s[0:1]
	v_mov_b32_e32 v67, 0x3ed96d27
	v_cmp_gt_u32_e32 vcc, s3, v0
	s_barrier
	s_nop 0
	v_cndmask_b32_e32 v72, 1.0, v67, vcc
	v_cndmask_b32_e32 v69, v75, v69, vcc
	v_cndmask_b32_e32 v68, v74, v68, vcc
	v_mov_b32_e32 v67, v71
	v_lshl_add_u64 v[74:75], v[68:69], 0, v[66:67]
	global_load_dwordx4 v[66:69], v[74:75], off
	global_load_dwordx4 v[78:81], v[74:75], off offset:32
	global_load_dwordx4 v[82:85], v[74:75], off offset:64
	global_load_dwordx4 v[86:89], v[74:75], off offset:96
	global_load_dwordx4 v[90:93], v[74:75], off offset:128
	global_load_dwordx4 v[94:97], v[74:75], off offset:160
	s_movk_i32 s0, 0x90
	v_mad_u32_u24 v71, v98, s0, 0
	global_load_dwordx4 v[98:101], v[74:75], off offset:192
	global_load_dwordx4 v[102:105], v[74:75], off offset:224
	v_lshlrev_b32_e32 v77, 3, v77
	v_mul_u32_u24_e32 v1, 0x90, v1
	v_add3_u32 v77, v71, v77, v1
	s_movk_i32 s0, 0xff
	v_add_u32_e32 v106, 0x1000, v77
	v_cmp_lt_u32_e64 s[0:1], s0, v0
	s_lshr_b32 s3, s2, 3
	s_and_b32 s3, s3, 0x3ffc
	s_lshl_b32 s2, s2, 13
	s_and_b32 s2, s2, 0x3e000
	s_waitcnt vmcnt(7)
	v_pk_add_f32 v[50:51], v[66:67], v[50:51]
	v_pk_add_f32 v[52:53], v[68:69], v[52:53]
	s_waitcnt vmcnt(6)
	v_pk_add_f32 v[54:55], v[78:79], v[54:55]
	v_pk_add_f32 v[56:57], v[80:81], v[56:57]
	s_waitcnt vmcnt(3)
	v_pk_add_f32 v[18:19], v[90:91], v[18:19]
	v_pk_add_f32 v[20:21], v[92:93], v[20:21]
	v_pk_add_f32 v[2:3], v[90:91], v[2:3]
	v_pk_add_f32 v[4:5], v[92:93], v[4:5]
	v_pk_mul_f32 v[18:19], v[72:73], v[18:19] op_sel_hi:[0,1]
	v_pk_mul_f32 v[20:21], v[72:73], v[20:21] op_sel_hi:[0,1]
	v_pk_mul_f32 v[2:3], v[72:73], v[2:3] op_sel_hi:[0,1]
	v_pk_mul_f32 v[4:5], v[72:73], v[4:5] op_sel_hi:[0,1]
	v_cvt_pk_f16_f32 v18, v18, v19
	v_cvt_pk_f16_f32 v19, v20, v21
	v_cvt_pk_f16_f32 v2, v2, v3
	v_cvt_pk_f16_f32 v3, v4, v5
	s_waitcnt vmcnt(2)
	v_pk_add_f32 v[4:5], v[94:95], v[22:23]
	v_pk_add_f32 v[20:21], v[96:97], v[24:25]
	v_pk_add_f32 v[58:59], v[82:83], v[58:59]
	v_pk_add_f32 v[60:61], v[84:85], v[60:61]
	v_pk_add_f32 v[62:63], v[86:87], v[62:63]
	v_pk_add_f32 v[64:65], v[88:89], v[64:65]
	v_pk_add_f32 v[34:35], v[66:67], v[34:35]
	v_pk_add_f32 v[36:37], v[68:69], v[36:37]
	v_pk_add_f32 v[38:39], v[78:79], v[38:39]
	v_pk_add_f32 v[40:41], v[80:81], v[40:41]
	v_pk_mul_f32 v[50:51], v[72:73], v[50:51] op_sel_hi:[0,1]
	v_pk_mul_f32 v[52:53], v[72:73], v[52:53] op_sel_hi:[0,1]
	v_pk_mul_f32 v[54:55], v[72:73], v[54:55] op_sel_hi:[0,1]
	v_pk_mul_f32 v[56:57], v[72:73], v[56:57] op_sel_hi:[0,1]
	v_pk_mul_f32 v[4:5], v[72:73], v[4:5] op_sel_hi:[0,1]
	v_pk_mul_f32 v[20:21], v[72:73], v[20:21] op_sel_hi:[0,1]
	v_pk_mul_f32 v[34:35], v[72:73], v[34:35] op_sel_hi:[0,1]
	v_pk_mul_f32 v[36:37], v[72:73], v[36:37] op_sel_hi:[0,1]
	v_pk_mul_f32 v[38:39], v[72:73], v[38:39] op_sel_hi:[0,1]
	v_pk_mul_f32 v[40:41], v[72:73], v[40:41] op_sel_hi:[0,1]
	v_pk_mul_f32 v[58:59], v[72:73], v[58:59] op_sel_hi:[0,1]
	v_pk_mul_f32 v[60:61], v[72:73], v[60:61] op_sel_hi:[0,1]
	v_pk_mul_f32 v[62:63], v[72:73], v[62:63] op_sel_hi:[0,1]
	v_pk_mul_f32 v[64:65], v[72:73], v[64:65] op_sel_hi:[0,1]
	v_cvt_pk_f16_f32 v50, v50, v51
	v_cvt_pk_f16_f32 v51, v52, v53
	v_cvt_pk_f16_f32 v52, v54, v55
	v_cvt_pk_f16_f32 v53, v56, v57
	v_cvt_pk_f16_f32 v4, v4, v5
	v_cvt_pk_f16_f32 v5, v20, v21
	v_cvt_pk_f16_f32 v34, v34, v35
	v_cvt_pk_f16_f32 v35, v36, v37
	v_cvt_pk_f16_f32 v36, v38, v39
	v_cvt_pk_f16_f32 v37, v40, v41
	v_cvt_pk_f16_f32 v38, v58, v59
	v_cvt_pk_f16_f32 v39, v60, v61
	v_cvt_pk_f16_f32 v40, v62, v63
	v_cvt_pk_f16_f32 v41, v64, v65
	ds_write2_b64 v77, v[50:51], v[52:53] offset1:2
	ds_write2_b64 v106, v[34:35], v[36:37] offset0:64 offset1:66
	ds_write2_b64 v77, v[38:39], v[40:41] offset0:4 offset1:6
	ds_write2_b64 v77, v[18:19], v[4:5] offset0:8 offset1:10
	v_pk_add_f32 v[0:1], v[94:95], v[6:7]
	v_pk_add_f32 v[4:5], v[96:97], v[8:9]
	v_pk_mul_f32 v[0:1], v[72:73], v[0:1] op_sel_hi:[0,1]
	v_pk_mul_f32 v[4:5], v[72:73], v[4:5] op_sel_hi:[0,1]
	v_cvt_pk_f16_f32 v0, v0, v1
	v_cvt_pk_f16_f32 v1, v4, v5
	ds_write2_b64 v106, v[2:3], v[0:1] offset0:72 offset1:74
	s_waitcnt vmcnt(1)
	v_pk_add_f32 v[0:1], v[98:99], v[26:27]
	v_pk_add_f32 v[2:3], v[100:101], v[28:29]
	v_pk_mul_f32 v[0:1], v[72:73], v[0:1] op_sel_hi:[0,1]
	v_pk_mul_f32 v[2:3], v[72:73], v[2:3] op_sel_hi:[0,1]
	v_cvt_pk_f16_f32 v0, v0, v1
	v_cvt_pk_f16_f32 v1, v2, v3
	v_pk_add_f32 v[2:3], v[98:99], v[10:11]
	v_pk_add_f32 v[4:5], v[100:101], v[12:13]
	v_pk_mul_f32 v[2:3], v[72:73], v[2:3] op_sel_hi:[0,1]
	v_pk_mul_f32 v[4:5], v[72:73], v[4:5] op_sel_hi:[0,1]
	v_cvt_pk_f16_f32 v2, v2, v3
	v_cvt_pk_f16_f32 v3, v4, v5
	s_waitcnt vmcnt(0)
	v_pk_add_f32 v[4:5], v[102:103], v[30:31]
	v_pk_add_f32 v[6:7], v[104:105], v[32:33]
	v_pk_mul_f32 v[4:5], v[72:73], v[4:5] op_sel_hi:[0,1]
	v_pk_mul_f32 v[6:7], v[72:73], v[6:7] op_sel_hi:[0,1]
	v_cvt_pk_f16_f32 v4, v4, v5
	v_cvt_pk_f16_f32 v5, v6, v7
	ds_write2_b64 v77, v[0:1], v[4:5] offset0:12 offset1:14
	v_pk_add_f32 v[0:1], v[102:103], v[14:15]
	v_pk_add_f32 v[4:5], v[104:105], v[16:17]
	v_pk_mul_f32 v[0:1], v[72:73], v[0:1] op_sel_hi:[0,1]
	v_pk_mul_f32 v[4:5], v[72:73], v[4:5] op_sel_hi:[0,1]
	v_cvt_pk_f16_f32 v0, v0, v1
	v_cvt_pk_f16_f32 v1, v4, v5
	ds_write2_b64 v106, v[2:3], v[0:1] offset0:76 offset1:78
	v_mov_b32_e32 v0, s12
	v_mov_b32_e32 v1, s6
	v_pk_add_f32 v[42:43], v[82:83], v[42:43]
	v_pk_add_f32 v[44:45], v[84:85], v[44:45]
	v_pk_add_f32 v[46:47], v[86:87], v[46:47]
	v_pk_add_f32 v[48:49], v[88:89], v[48:49]
	v_cndmask_b32_e32 v0, v0, v1, vcc
	v_mov_b32_e32 v1, s13
	v_mov_b32_e32 v2, s7
	v_and_or_b32 v4, v76, 3, s3
	v_pk_mul_f32 v[42:43], v[72:73], v[42:43] op_sel_hi:[0,1]
	v_pk_mul_f32 v[44:45], v[72:73], v[44:45] op_sel_hi:[0,1]
	v_pk_mul_f32 v[46:47], v[72:73], v[46:47] op_sel_hi:[0,1]
	v_pk_mul_f32 v[48:49], v[72:73], v[48:49] op_sel_hi:[0,1]
	v_cndmask_b32_e32 v1, v1, v2, vcc
	v_lshl_or_b32 v4, v4, 18, s2
	v_cvt_pk_f16_f32 v42, v42, v43
	v_cvt_pk_f16_f32 v43, v44, v45
	v_cvt_pk_f16_f32 v44, v46, v47
	v_cvt_pk_f16_f32 v45, v48, v49
	v_and_b32_e32 v1, 0xffff, v1
	v_mov_b32_e32 v2, 0x800000
	v_mov_b32_e32 v3, 0x20000
	v_lshl_or_b32 v8, v73, 4, v4
	ds_write2_b64 v106, v[42:43], v[44:45] offset0:68 offset1:70
	s_and_saveexec_b64 s[2:3], s[0:1]
	s_xor_b64 s[2:3], exec, s[2:3]
	s_cbranch_execz .LBB1_18
	v_lshrrev_b32_e32 v4, 2, v73
	v_mul_u32_u24_e32 v4, 0x90, v4
	v_and_b32_e32 v5, 48, v70
	v_add3_u32 v9, v71, v4, v5
	ds_read_b128 v[4:7], v9
	s_mov_b64 s[8:9], exec

	.amdhsa_kernel _Z11proj_kernelPKfS0_PKDF16_S0_S0_PDF16_S3_
		.amdhsa_group_segment_fixed_size 0
		.amdhsa_private_segment_fixed_size 0
		.amdhsa_kernarg_size 56
		.amdhsa_user_sgpr_count 2
		.amdhsa_user_sgpr_dispatch_ptr 0
		.amdhsa_user_sgpr_queue_ptr 0
		.amdhsa_user_sgpr_kernarg_segment_ptr 1
		.amdhsa_user_sgpr_dispatch_id 0
		.amdhsa_user_sgpr_kernarg_preload_length 0
		.amdhsa_user_sgpr_kernarg_preload_offset 0
		.amdhsa_user_sgpr_private_segment_size 0
		.amdhsa_uses_dynamic_stack 0
		.amdhsa_enable_private_segment 0
		.amdhsa_system_sgpr_workgroup_id_x 1
		.amdhsa_system_sgpr_workgroup_id_y 0
		.amdhsa_system_sgpr_workgroup_id_z 0
		.amdhsa_system_sgpr_workgroup_info 0
		.amdhsa_system_vgpr_workitem_id 0
		.amdhsa_next_free_vgpr 170
		.amdhsa_next_free_sgpr 16
		.amdhsa_accum_offset 172
		.amdhsa_reserve_vcc 1
		.amdhsa_float_round_mode_32 0
		.amdhsa_float_round_mode_16_64 0
		.amdhsa_float_denorm_mode_32 3
		.amdhsa_float_denorm_mode_16_64 3
		.amdhsa_dx10_clamp 1
		.amdhsa_ieee_mode 1
		.amdhsa_fp16_overflow 0
		.amdhsa_tg_split 0
		.amdhsa_exception_fp_ieee_invalid_op 0
		.amdhsa_exception_fp_denorm_src 0
		.amdhsa_exception_fp_ieee_div_zero 0
		.amdhsa_exception_fp_ieee_overflow 0
		.amdhsa_exception_fp_ieee_underflow 0
		.amdhsa_exception_fp_ieee_inexact 0
		.amdhsa_exception_int_div_zero 0
	.end_amdhsa_kernel

amdhsa.kernels:
  - .agpr_count:     0
    .args:
      - .actual_access:  read_only
        .address_space:  global
        .offset:         0
        .size:           8
        .value_kind:     global_buffer
      - .actual_access:  read_only
        .address_space:  global
        .offset:         8
        .size:           8
        .value_kind:     global_buffer
      - .actual_access:  read_only
        .address_space:  global
        .offset:         16
        .size:           8
        .value_kind:     global_buffer
      - .actual_access:  read_only
        .address_space:  global
        .offset:         24
        .size:           8
        .value_kind:     global_buffer
      - .actual_access:  read_only
        .address_space:  global
        .offset:         32
        .size:           8
        .value_kind:     global_buffer
      - .actual_access:  write_only
        .address_space:  global
        .offset:         40
        .size:           8
        .value_kind:     global_buffer
      - .actual_access:  write_only
        .address_space:  global
        .offset:         48
        .size:           8
        .value_kind:     global_buffer
      - .actual_access:  write_only
        .address_space:  global
        .offset:         56
        .size:           8
        .value_kind:     global_buffer
      - .actual_access:  write_only
        .address_space:  global
        .offset:         64
        .size:           8
        .value_kind:     global_buffer
    .group_segment_fixed_size: 0
    .kernarg_segment_align: 8
    .kernarg_segment_size: 72
    .language:       OpenCL C
    .language_version:
      - 2
      - 0
    .max_flat_workgroup_size: 256
    .name:           _Z11prep_kernelPKfS0_S0_S0_S0_PDF16_S1_S1_S1_
    .private_segment_fixed_size: 0
    .sgpr_count:     21
    .sgpr_spill_count: 0
    .symbol:         _Z11prep_kernelPKfS0_S0_S0_S0_PDF16_S1_S1_S1_.kd
    .uniform_work_group_size: 1
    .uses_dynamic_stack: false
    .vgpr_count:     18
    .vgpr_spill_count: 0
    .wavefront_size: 64
  - .agpr_count:     0
    .args:
      - .actual_access:  read_only
        .address_space:  global
        .offset:         0
        .size:           8
        .value_kind:     global_buffer
      - .actual_access:  read_only
        .address_space:  global
        .offset:         8
        .size:           8
        .value_kind:     global_buffer
      - .actual_access:  read_only
        .address_space:  global
        .offset:         16
        .size:           8
        .value_kind:     global_buffer
      - .actual_access:  read_only
        .address_space:  global
        .offset:         24
        .size:           8
        .value_kind:     global_buffer
      - .actual_access:  read_only
        .address_space:  global
        .offset:         32
        .size:           8
        .value_kind:     global_buffer
      - .actual_access:  write_only
        .address_space:  global
        .offset:         40
        .size:           8
        .value_kind:     global_buffer
      - .actual_access:  write_only
        .address_space:  global
        .offset:         48
        .size:           8
        .value_kind:     global_buffer
    .group_segment_fixed_size: 0
    .kernarg_segment_align: 8
    .kernarg_segment_size: 56
    .language:       OpenCL C
    .language_version:
      - 2
      - 0
    .max_flat_workgroup_size: 512
    .name:           _Z11proj_kernelPKfS0_PKDF16_S0_S0_PDF16_S3_
    .private_segment_fixed_size: 0
    .sgpr_count:     22
    .sgpr_spill_count: 0
    .symbol:         _Z11proj_kernelPKfS0_PKDF16_S0_S0_PDF16_S3_.kd
    .uniform_work_group_size: 1
    .uses_dynamic_stack: false
    .vgpr_count:     170
    .vgpr_spill_count: 0
    .wavefront_size: 64
  - .agpr_count:     0
    .args:
      - .address_space:  global
        .offset:         0
        .size:           8
        .value_kind:     global_buffer
      - .address_space:  global
        .offset:         8
        .size:           8
        .value_kind:     global_buffer
      - .actual_access:  write_only
        .address_space:  global
        .offset:         16
        .size:           8
        .value_kind:     global_buffer
    .group_segment_fixed_size: 0
    .kernarg_segment_align: 8
    .kernarg_segment_size: 24
    .language:       OpenCL C
    .language_version:
      - 2
      - 0
    .max_flat_workgroup_size: 512
    .name:           _Z11attn_kernelPKDF16_S0_PDF16_
    .private_segment_fixed_size: 0
    .sgpr_count:     56
    .sgpr_spill_count: 0
    .symbol:         _Z11attn_kernelPKDF16_S0_PDF16_.kd
    .uniform_work_group_size: 1
    .uses_dynamic_stack: false
    .vgpr_count:     192
    .vgpr_spill_count: 0
    .wavefront_size: 64
  - .agpr_count:     0
    .args:
      - .actual_access:  read_only
        .address_space:  global
        .offset:         0
        .size:           8
        .value_kind:     global_buffer
      - .actual_access:  read_only
        .address_space:  global
        .offset:         8
        .size:           8
        .value_kind:     global_buffer
      - .actual_access:  read_only
        .address_space:  global
        .offset:         16
        .size:           8
        .value_kind:     global_buffer
      - .actual_access:  read_only
        .address_space:  global
        .offset:         24
        .size:           8
        .value_kind:     global_buffer
      - .actual_access:  read_only
        .address_space:  global
        .offset:         32
        .size:           8
        .value_kind:     global_buffer
      - .address_space:  global
        .offset:         40
        .size:           8
        .value_kind:     global_buffer
      - .actual_access:  read_only
        .address_space:  global
        .offset:         48
        .size:           8
        .value_kind:     global_buffer
      - .actual_access:  read_only
        .address_space:  global
        .offset:         56
        .size:           8
        .value_kind:     global_buffer
      - .actual_access:  read_only
        .address_space:  global
        .offset:         64
        .size:           8
        .value_kind:     global_buffer
      - .address_space:  global
        .offset:         72
        .size:           8
        .value_kind:     global_buffer
      - .actual_access:  read_only
        .address_space:  global
        .offset:         80
        .size:           8
        .value_kind:     global_buffer
      - .actual_access:  write_only
        .address_space:  global
        .offset:         88
        .size:           8
        .value_kind:     global_buffer
    .group_segment_fixed_size: 0
    .kernarg_segment_align: 8
    .kernarg_segment_size: 96
    .language:       OpenCL C
    .language_version:
      - 2
      - 0
    .max_flat_workgroup_size: 512
    .name:           _Z10ffn_kernelPKfS0_PKDF16_S2_S0_S2_S0_S0_S0_S2_S0_Pf
    .private_segment_fixed_size: 0
    .sgpr_count:     24
    .sgpr_spill_count: 0
    .symbol:         _Z10ffn_kernelPKfS0_PKDF16_S2_S0_S2_S0_S0_S0_S2_S0_Pf.kd
    .uniform_work_group_size: 1
    .uses_dynamic_stack: false
    .vgpr_count:     230
    .vgpr_spill_count: 0
    .wavefront_size: 64
